# expert-weight conversion re-slotted: the 12 percent that ran beside the layer-0 out-projection GEMM (most memory interference) moves into the layer-1 scan slot
# baseline (speedup 1.0000x reference)
.LBB0_1248:
	s_abs_i32 s2, s90
	s_waitcnt vmcnt(0)
	v_cvt_f32_u32_e32 v2, s2
	s_sub_i32 s3, 0, s2
	v_rcp_iflag_f32_e32 v2, v2
	s_nop 0
	v_mul_f32_e32 v2, 0x4f7ffffe, v2
	v_cvt_u32_f32_e32 v2, v2
	s_nop 0
	v_readfirstlane_b32 s4, v2
	s_mul_i32 s3, s3, s4
	s_mul_hi_u32 s3, s4, s3
	s_add_i32 s4, s4, s3
	s_mul_hi_u32 s3, s4, 0x480
	s_mul_i32 s3, s3, s2
	s_sub_i32 s3, 0x480, s3
	s_sub_i32 s4, s3, s2
	s_cmp_ge_u32 s3, s2
	s_cselect_b32 s3, s4, s3
	s_sub_i32 s4, s3, s2
	s_cmp_ge_u32 s3, s2
	s_cselect_b32 s4, s4, s3
	s_cmp_eq_u32 s4, 0
	s_cselect_b64 s[2:3], -1, 0
	s_cmp_lt_i32 s88, s4
	s_cselect_b64 s[6:7], -1, 0
	s_or_b64 s[2:3], s[2:3], s[6:7]
	s_and_b64 vcc, exec, s[2:3]
	s_branch .LBB0_1296
	s_sub_i32 s2, s88, s4
	s_lshl_b32 s2, s2, 3
	s_add_i32 s2, s2, s83
	s_cmpk_gt_u32 s2, 0x1fad
	s_cbranch_scc1 .LBB0_1296
	s_sub_i32 s3, s90, s4
	s_lshl_b32 s5, s3, 3
	s_mul_i32 s3, s83, 0x4200
	s_add_i32 s6, s3, 0
	s_add_i32 s12, s2, 0x4200
	s_add_u32 s13, s86, 0x29400000
	s_addc_u32 s14, s87, 0
	s_add_u32 s15, s86, 0x13400000
	s_load_dwordx2 s[2:3], s[74:75], 0xf0
	v_and_b32_e32 v2, 7, v0
	v_lshrrev_b32_e32 v73, 3, v162
	s_addc_u32 s16, s87, 0
	v_lshlrev_b32_e32 v72, 2, v2
	v_lshlrev_b32_e32 v66, 4, v2
	v_mul_u32_u24_e32 v2, 0x840, v2
	v_lshlrev_b32_e32 v5, 2, v73
	s_add_u32 s17, s86, 0x960000
	v_add_u32_e32 v3, s6, v66
	v_mul_u32_u24_e32 v4, 0x84, v73
	v_add3_u32 v77, s6, v2, v5
	s_addc_u32 s18, s87, 0
	s_lshl_b32 s6, s90, 8
	s_lshl_b32 s7, s4, 8
	v_mov_b32_e32 v69, 0
	s_sub_i32 s20, s6, s7
	s_lshl_b32 s6, s90, 4
	s_lshl_b32 s4, s4, 4
	v_add_u32_e32 v78, v3, v4
	v_or_b32_e32 v74, 8, v73
	v_or_b32_e32 v75, 16, v73
	v_or_b32_e32 v76, 24, v73
	v_mov_b32_e32 v67, v69
	s_lshl_b32 s19, s12, 5
	s_lshl_b32 s21, s12, 1
	s_sub_i32 s22, s6, s4
	s_mov_b32 s4, 0x43800000
	v_add_u32_e32 v79, 0x420, v78
	v_add_u32_e32 v80, 0x428, v78
	v_add_u32_e32 v81, 0x840, v78
	v_add_u32_e32 v82, 0x848, v78
	v_add_u32_e32 v83, 0xc60, v78
	v_add_u32_e32 v84, 0xc68, v78
	v_add_u32_e32 v85, 0x1080, v78
	v_add_u32_e32 v86, 0x1088, v78
	v_add_u32_e32 v87, 0x14a0, v78
	v_add_u32_e32 v88, 0x14a8, v78
	v_add_u32_e32 v89, 0x18c0, v78
	v_add_u32_e32 v90, 0x18c8, v78
	v_add_u32_e32 v91, 0x1ce0, v78
	v_add_u32_e32 v92, 0x1ce8, v78
	v_add_u32_e32 v93, 0x2100, v78
	v_add_u32_e32 v94, 0x2108, v78
	v_add_u32_e32 v95, 0x2520, v78
	v_add_u32_e32 v96, 0x2528, v78
	v_add_u32_e32 v97, 0x2940, v78
	v_add_u32_e32 v98, 0x2948, v78
	v_add_u32_e32 v99, 0x2d60, v78
	v_add_u32_e32 v100, 0x2d68, v78
	v_add_u32_e32 v101, 0x3180, v78
	v_add_u32_e32 v102, 0x3188, v78
	v_add_u32_e32 v103, 0x35a0, v78
	v_add_u32_e32 v104, 0x35a8, v78
	v_add_u32_e32 v105, 0x39c0, v78
	v_add_u32_e32 v106, 0x39c8, v78
	v_add_u32_e32 v107, 0x3de0, v78
	v_add_u32_e32 v108, 0x3de8, v78
	s_mov_b32 s23, 0xc3e00000
	s_movk_i32 s24, 0x1600
	s_movk_i32 s25, 0xe8
	s_movk_i32 s26, 0x5800
	v_add_u32_e32 v109, 0x400, v77
	v_mov_b32_e32 v110, 0x43e00000
	v_add_u32_e32 v111, 0x600, v77
	s_branch .LBB0_1253

.LBB0_1544:
	s_abs_i32 s2, s90
	s_waitcnt vmcnt(0)
	v_cvt_f32_u32_e32 v2, s2
	s_sub_i32 s3, 0, s2
	v_rcp_iflag_f32_e32 v2, v2
	s_nop 0
	v_mul_f32_e32 v2, 0x4f7ffffe, v2
	v_cvt_u32_f32_e32 v2, v2
	s_nop 0
	v_readfirstlane_b32 s4, v2
	s_mul_i32 s3, s3, s4
	s_mul_hi_u32 s3, s4, s3
	s_add_i32 s4, s4, s3
	s_mul_hi_u32 s3, s4, 0x480
	s_mul_i32 s3, s3, s2
	s_sub_i32 s3, 0x480, s3
	s_sub_i32 s4, s3, s2
	s_cmp_ge_u32 s3, s2
	s_cselect_b32 s3, s4, s3
	s_sub_i32 s4, s3, s2
	s_cmp_ge_u32 s3, s2
	s_cselect_b32 s4, s4, s3
	s_cmp_eq_u32 s4, 0
	s_cselect_b64 s[2:3], -1, 0
	s_cmp_lt_i32 s88, s4
	s_cselect_b64 s[6:7], -1, 0
	s_or_b64 s[2:3], s[2:3], s[6:7]
	s_and_b64 vcc, exec, s[2:3]
	s_cbranch_vccnz .LBB0_1592
	s_sub_i32 s2, s88, s4
	s_lshl_b32 s2, s2, 3
	s_add_i32 s2, s2, s83
	s_cmpk_gt_u32 s2, 0x41ff
	s_cbranch_scc1 .LBB0_1592
	s_sub_i32 s3, s90, s4
	s_lshl_b32 s5, s3, 3
	s_mul_i32 s3, s83, 0x4200
	s_add_i32 s6, s3, 0
	s_add_i32 s12, s2, 0x4200
	s_add_u32 s13, s86, 0x29400000
	s_addc_u32 s14, s87, 0
	s_add_u32 s15, s86, 0x13400000
	s_load_dwordx2 s[2:3], s[74:75], 0xf0
	v_and_b32_e32 v2, 7, v0
	v_lshrrev_b32_e32 v73, 3, v162
	s_addc_u32 s16, s87, 0
	v_lshlrev_b32_e32 v72, 2, v2
	v_lshlrev_b32_e32 v66, 4, v2
	v_mul_u32_u24_e32 v2, 0x840, v2
	v_lshlrev_b32_e32 v5, 2, v73
	s_add_u32 s17, s86, 0x960000
	v_add_u32_e32 v3, s6, v66
	v_mul_u32_u24_e32 v4, 0x84, v73
	v_add3_u32 v77, s6, v2, v5
	s_addc_u32 s18, s87, 0
	s_lshl_b32 s6, s90, 8
	s_lshl_b32 s7, s4, 8
	v_mov_b32_e32 v69, 0
	s_sub_i32 s20, s6, s7
	s_lshl_b32 s6, s90, 4
	s_lshl_b32 s4, s4, 4
	v_add_u32_e32 v78, v3, v4
	v_or_b32_e32 v74, 8, v73
	v_or_b32_e32 v75, 16, v73
	v_or_b32_e32 v76, 24, v73
	v_mov_b32_e32 v67, v69
	s_lshl_b32 s19, s12, 5
	s_lshl_b32 s21, s12, 1
	s_sub_i32 s22, s6, s4
	s_mov_b32 s4, 0x43800000
	v_add_u32_e32 v79, 0x420, v78
	v_add_u32_e32 v80, 0x428, v78
	v_add_u32_e32 v81, 0x840, v78
	v_add_u32_e32 v82, 0x848, v78
	v_add_u32_e32 v83, 0xc60, v78
	v_add_u32_e32 v84, 0xc68, v78
	v_add_u32_e32 v85, 0x1080, v78
	v_add_u32_e32 v86, 0x1088, v78
	v_add_u32_e32 v87, 0x14a0, v78
	v_add_u32_e32 v88, 0x14a8, v78
	v_add_u32_e32 v89, 0x18c0, v78
	v_add_u32_e32 v90, 0x18c8, v78
	v_add_u32_e32 v91, 0x1ce0, v78
	v_add_u32_e32 v92, 0x1ce8, v78
	v_add_u32_e32 v93, 0x2100, v78
	v_add_u32_e32 v94, 0x2108, v78
	v_add_u32_e32 v95, 0x2520, v78
	v_add_u32_e32 v96, 0x2528, v78
	v_add_u32_e32 v97, 0x2940, v78
	v_add_u32_e32 v98, 0x2948, v78
	v_add_u32_e32 v99, 0x2d60, v78
	v_add_u32_e32 v100, 0x2d68, v78
	v_add_u32_e32 v101, 0x3180, v78
	v_add_u32_e32 v102, 0x3188, v78
	v_add_u32_e32 v103, 0x35a0, v78
	v_add_u32_e32 v104, 0x35a8, v78
	v_add_u32_e32 v105, 0x39c0, v78
	v_add_u32_e32 v106, 0x39c8, v78
	v_add_u32_e32 v107, 0x3de0, v78
	v_add_u32_e32 v108, 0x3de8, v78
	s_mov_b32 s23, 0xc3e00000
	s_movk_i32 s24, 0x1600
	s_movk_i32 s25, 0xe8
	s_movk_i32 s26, 0x5800
	v_add_u32_e32 v109, 0x400, v77
	v_mov_b32_e32 v110, 0x43e00000
	v_add_u32_e32 v111, 0x600, v77
	s_branch .LBB0_1549

.LBB0_1548:
	s_add_i32 s12, s12, s5
	s_add_i32 s19, s19, s20
	s_add_i32 s21, s21, s22
	s_cmp_lt_i32 s12, 0x8400
	s_cbranch_scc0 .LBB0_1592

.LBB0_2043:
	v_readlane_b32 s74, v254, 10
	v_readlane_b32 s75, v254, 11
	v_readlane_b32 s90, v254, 16
	s_load_dwordx4 s[84:87], s[74:75], 0xf8
	s_sub_i32 s0, 0x180, s90
	s_cmpk_lt_i32 s90, 0x180
	s_cselect_b32 s0, s0, 0
	v_readlane_b32 s88, v254, 18
	s_cmp_lt_i32 s88, s0
	v_readlane_b32 s83, v254, 14
	v_readlane_b32 s92, v254, 15
	s_waitcnt vmcnt(0) lgkmcnt(0)
	s_barrier
	v_readlane_b32 s91, v254, 17
	v_readlane_b32 s89, v254, 19
	s_cbranch_scc1 .LBB0_2091
	s_sub_i32 s1, s88, s0
	s_lshl_b32 s1, s1, 3
	s_add_i32 s1, s1, s83
	s_cmpk_gt_u32 s1, 0x83ff
	s_cbranch_scc1 .LBB0_2091
	s_sub_i32 s0, s90, s0
	s_lshl_b32 s3, s0, 3
	s_mul_i32 s0, s83, 0x4200
	s_add_i32 s2, s0, 0
	s_add_i32 s4, s1, 0x8400
	s_add_u32 s10, s86, 0x29400000
	s_addc_u32 s11, s87, 0
	s_add_u32 s12, s86, 0x13400000
	v_and_b32_e32 v2, 7, v0
	v_lshrrev_b32_e32 v73, 3, v162
	s_addc_u32 s13, s87, 0
	v_lshlrev_b32_e32 v72, 2, v2
	v_lshlrev_b32_e32 v66, 4, v2
	v_mul_u32_u24_e32 v2, 0x840, v2
	v_lshlrev_b32_e32 v5, 2, v73
	s_add_u32 s14, s86, 0x960000
	v_add_u32_e32 v3, s2, v66
	v_add3_u32 v77, s2, v2, v5
	s_addc_u32 s15, s87, 0
	s_lshl_b32 s2, s90, 3
	s_lshl_b32 s5, s88, 3
	s_load_dwordx2 s[0:1], s[74:75], 0xf0
	s_add_i32 s2, s2, s5
	s_max_i32 s5, s90, 0x180
	s_lshl_b32 s6, s5, 3
	v_mul_u32_u24_e32 v4, 0x84, v73
	s_sub_i32 s16, s2, s6
	s_lshl_b32 s2, s90, 9
	s_lshl_b32 s6, s5, 8
	v_mov_b32_e32 v69, 0
	s_lshl_b32 s18, s4, 5
	s_sub_i32 s19, s2, s6
	s_lshl_b32 s20, s4, 1
	s_lshl_b32 s2, s90, 5
	s_lshl_b32 s4, s5, 4
	v_add_u32_e32 v78, v3, v4
	v_or_b32_e32 v74, 8, v73
	v_or_b32_e32 v75, 16, v73
	v_or_b32_e32 v76, 24, v73
	v_mov_b32_e32 v67, v69
	s_add_i32 s17, s83, 0x8400
	s_sub_i32 s21, s2, s4
	s_mov_b32 s2, 0x43800000
	v_add_u32_e32 v79, 0x420, v78
	v_add_u32_e32 v80, 0x428, v78
	v_add_u32_e32 v81, 0x840, v78
	v_add_u32_e32 v82, 0x848, v78
	v_add_u32_e32 v83, 0xc60, v78
	v_add_u32_e32 v84, 0xc68, v78
	v_add_u32_e32 v85, 0x1080, v78
	v_add_u32_e32 v86, 0x1088, v78
	v_add_u32_e32 v87, 0x14a0, v78
	v_add_u32_e32 v88, 0x14a8, v78
	v_add_u32_e32 v89, 0x18c0, v78
	v_add_u32_e32 v90, 0x18c8, v78
	v_add_u32_e32 v91, 0x1ce0, v78
	v_add_u32_e32 v92, 0x1ce8, v78
	v_add_u32_e32 v93, 0x2100, v78
	v_add_u32_e32 v94, 0x2108, v78
	v_add_u32_e32 v95, 0x2520, v78
	v_add_u32_e32 v96, 0x2528, v78
	v_add_u32_e32 v97, 0x2940, v78
	v_add_u32_e32 v98, 0x2948, v78
	v_add_u32_e32 v99, 0x2d60, v78
	v_add_u32_e32 v100, 0x2d68, v78
	v_add_u32_e32 v101, 0x3180, v78
	v_add_u32_e32 v102, 0x3188, v78
	v_add_u32_e32 v103, 0x35a0, v78
	v_add_u32_e32 v104, 0x35a8, v78
	v_add_u32_e32 v105, 0x39c0, v78
	v_add_u32_e32 v106, 0x39c8, v78
	v_add_u32_e32 v107, 0x3de0, v78
	v_add_u32_e32 v108, 0x3de8, v78
	s_mov_b32 s22, 0xc3e00000
	s_movk_i32 s23, 0x1600
	s_movk_i32 s24, 0xe8
	s_movk_i32 s25, 0x5800
	v_add_u32_e32 v109, 0x400, v77
	v_mov_b32_e32 v110, 0x43e00000
	v_add_u32_e32 v111, 0x600, v77
	s_branch .LBB0_2048
